# v21 + grid barrier release: everyone waits for the TOP arrival counter to reach (gen+1)*nx (no separate generation word round trip), barriers 1..11
# speedup vs baseline: 1.0180x; 1.0180x over previous
.LBB0_92:
	s_or_b64 exec, exec, s[8:9]
	v_cvt_f32_u32_e32 v5, v3
	s_waitcnt vmcnt(0)
	v_readfirstlane_b32 s6, v4
	v_sub_u32_e32 v4, 0, v3
	v_rcp_iflag_f32_e32 v5, v5
	v_add_u32_e32 v6, s6, v2
	v_mul_f32_e32 v5, 0x4f7ffffe, v5
	v_cvt_u32_f32_e32 v5, v5
	v_mul_lo_u32 v2, v4, v5
	v_mul_hi_u32 v2, v5, v2
	v_add_u32_e32 v2, v5, v2
	v_mul_hi_u32 v2, v6, v2
	v_mul_lo_u32 v4, v2, v3
	v_sub_u32_e32 v4, v6, v4
	v_add_u32_e32 v5, 1, v2
	v_cmp_ge_u32_e32 vcc, v4, v3
	s_nop 1
	v_cndmask_b32_e32 v2, v2, v5, vcc
	v_sub_u32_e32 v5, v4, v3
	v_cndmask_b32_e32 v4, v4, v5, vcc
	v_add_u32_e32 v5, 1, v2
	v_cmp_ge_u32_e32 vcc, v4, v3
	v_add_u32_e32 v4, 1, v6
	s_nop 0
	v_cndmask_b32_e32 v2, v2, v5, vcc
	v_mul_lo_u32 v5, v3, v2
	v_add_u32_e32 v3, v5, v3
	v_cmp_ne_u32_e32 vcc, v4, v3
	s_and_saveexec_b64 s[6:7], vcc
	s_xor_b64 s[6:7], exec, s[6:7]
	s_cbranch_execz .LBB0_106
	s_waitcnt lgkmcnt(0)
	v_add_u32_e32 v5, 1, v2
	v_mul_lo_u32 v5, v5, v1
	v_mov_b32_e32 v1, 0x7000
	global_load_dword v1, v1, s[50:51] offset:1024 sc1
	s_add_u32 s12, s50, 0x7400
	s_addc_u32 s13, s51, 0
	s_waitcnt vmcnt(0)
	v_cmp_lt_u32_e32 vcc, v1, v5
	s_and_saveexec_b64 s[8:9], vcc
	s_cbranch_execz .LBB0_105
	s_add_u32 s10, s50, 0x4200
	s_addc_u32 s11, s51, 0
	s_mov_b32 s24, 1
	s_mov_b64 s[14:15], 0
	v_mov_b32_e32 v1, 0
	s_branch .LBB0_96

.LBB0_98:
	global_load_dword v3, v1, s[12:13] sc1
	s_add_i32 s24, s24, 1
	s_mov_b64 s[20:21], -1
	s_waitcnt vmcnt(0)
	v_cmp_ge_u32_e32 vcc, v3, v5
	s_orn2_b64 s[18:19], vcc, exec
	s_branch .LBB0_95

.LBB0_109:
	s_or_b64 exec, exec, s[8:9]
	v_cvt_f32_u32_e32 v4, v1
	s_waitcnt vmcnt(0)
	v_readfirstlane_b32 s6, v3
	s_add_u32 s8, s50, 0x7500
	s_addc_u32 s9, s51, 0
	v_rcp_iflag_f32_e32 v4, v4
	v_add_u32_e32 v2, s6, v2
	v_add_u32_e32 v5, 1, v2
	s_mov_b64 s[10:11], -1
	v_mul_f32_e32 v3, 0x4f7ffffe, v4
	v_cvt_u32_f32_e32 v3, v3
	v_sub_u32_e32 v4, 0, v1
	v_mul_lo_u32 v4, v4, v3
	v_mul_hi_u32 v4, v3, v4
	v_add_u32_e32 v3, v3, v4
	v_mul_hi_u32 v3, v2, v3
	v_mul_lo_u32 v4, v3, v1
	v_sub_u32_e32 v2, v2, v4
	v_add_u32_e32 v6, 1, v3
	v_cmp_ge_u32_e32 vcc, v2, v1
	v_sub_u32_e32 v4, v2, v1
	s_nop 0
	v_cndmask_b32_e32 v3, v3, v6, vcc
	v_cndmask_b32_e32 v2, v2, v4, vcc
	v_add_u32_e32 v4, 1, v3
	v_cmp_ge_u32_e32 vcc, v2, v1
	s_nop 1
	v_cndmask_b32_e32 v4, v3, v4, vcc
	v_mul_lo_u32 v2, v1, v4
	v_add_u32_e32 v1, v2, v1
	v_cmp_ne_u32_e32 vcc, v5, v1
	v_mov_b64_e32 v[2:3], s[8:9]
	s_and_saveexec_b64 s[6:7], vcc
	s_cbranch_execz .LBB0_121
	v_mov_b32_e32 v5, v1
	s_add_u32 s100, s50, 0x7400
	s_addc_u32 s101, s51, 0
	v_mov_b32_e32 v1, 0
	global_load_dword v2, v1, s[100:101] sc1
	s_mov_b64 s[14:15], 0
	s_waitcnt vmcnt(0)
	v_cmp_lt_u32_e32 vcc, v2, v5
	s_and_saveexec_b64 s[12:13], vcc
	s_cbranch_execz .LBB0_120
	s_add_u32 s10, s50, 0x4200
	s_addc_u32 s11, s51, 0
	s_mov_b32 s24, 1
	s_branch .LBB0_113

.LBB0_115:
	global_load_dword v2, v1, s[100:101] sc1
	s_add_i32 s24, s24, 1
	s_mov_b64 s[18:19], -1
	s_waitcnt vmcnt(0)
	v_cmp_ge_u32_e32 vcc, v2, v5
	s_orn2_b64 s[22:23], vcc, exec
	s_branch .LBB0_112
